# baseline (speedup 1.0000x reference)
.Lfc_h1_entry:
	s_setprio 1
	s_add_u32 m0, s22, 0x0
	s_nop 0
	global_load_lds_dwordx4 v5, s[24:25]
	s_add_u32 m0, s22, 0x400
	s_nop 0
	global_load_lds_dwordx4 v6, s[24:25]
	s_add_u32 m0, s23, 0x0
	s_nop 0
	global_load_lds_dwordx4 v11, s[28:29]
	s_add_u32 m0, s23, 0x400
	s_nop 0
	global_load_lds_dwordx4 v11, s[32:33]
	s_add_u32 m0, s23, 0x800
	s_nop 0
	global_load_lds_dwordx4 v11, s[36:37]
	s_add_u32 s24, s24, 0x80
	s_addc_u32 s25, s25, 0
	s_add_u32 s28, s28, 0x30000
	s_addc_u32 s29, s29, 0
	s_add_u32 s32, s32, 0x30000
	s_addc_u32 s33, s33, 0
	s_add_u32 s36, s36, 0x30000
	s_addc_u32 s37, s37, 0
	s_add_u32 m0, s22, 0xa000
	s_nop 0
	global_load_lds_dwordx4 v5, s[26:27]
	s_add_u32 m0, s22, 0xa400
	s_nop 0
	global_load_lds_dwordx4 v6, s[26:27]
	s_add_u32 m0, s23, 0xa000
	s_nop 0
	global_load_lds_dwordx4 v11, s[30:31]
	s_add_u32 m0, s23, 0xa400
	s_nop 0
	global_load_lds_dwordx4 v11, s[34:35]
	s_add_u32 m0, s23, 0xa800
	s_nop 0
	global_load_lds_dwordx4 v11, s[38:39]
	s_add_u32 s26, s26, 0x80
	s_addc_u32 s27, s27, 0
	s_add_u32 s30, s30, 0x30000
	s_addc_u32 s31, s31, 0
	s_add_u32 s34, s34, 0x30000
	s_addc_u32 s35, s35, 0
	s_add_u32 s38, s38, 0x30000
	s_addc_u32 s39, s39, 0
	s_waitcnt vmcnt(10)
	v_med3_i32 v64, v64, 0, s93
	v_med3_i32 v65, v65, 1, s94
	v_med3_i32 v66, v66, 0, s93
	v_med3_i32 v67, v67, 1, s94
	v_add_u32_e32 v64, s92, v64
	v_add_u32_e32 v66, s92, v66
	v_add_u32_e32 v65, s92, v65
	v_add_u32_e32 v67, s92, v67
	v_add_u32_e32 v65, -1, v65
	v_add_u32_e32 v67, -1, v67
	v_lshl_add_u32 v7, v64, 10, v71
	v_lshl_add_u32 v8, v66, 10, v71
	v_lshl_add_u32 v9, v65, 10, v71
	v_lshl_add_u32 v10, v67, 10, v71
	v_cvt_pk_f16_f32 v12, v40, v41
	v_cvt_pk_f16_f32 v13, v42, v43
	v_cvt_pk_f16_f32 v14, v44, v45
	v_cvt_pk_f16_f32 v15, v46, v47
	v_cvt_pk_f16_f32 v56, v56, v57
	v_cvt_pk_f16_f32 v57, v58, v59
	v_cvt_pk_f16_f32 v58, v60, v61
	v_cvt_pk_f16_f32 v59, v62, v63
	v_cvt_pk_f16_f32 v60, v48, v49
	v_cvt_pk_f16_f32 v61, v50, v51
	v_cvt_pk_f16_f32 v62, v52, v53
	v_cvt_pk_f16_f32 v63, v54, v55
	v_mov_b32_e32 v64, v16
	v_mov_b32_e32 v65, v17
	v_mov_b32_e32 v66, v18
	v_mov_b32_e32 v67, v19
	v_mov_b32_e32 v68, v20
	v_mov_b32_e32 v69, v21
	v_mov_b32_e32 v70, v22
	v_mov_b32_e32 v71, v23
	v_mov_b32_e32 v72, v24
	v_mov_b32_e32 v73, v25
	v_mov_b32_e32 v74, v26
	v_mov_b32_e32 v75, v27
	v_mov_b32_e32 v76, v28
	v_mov_b32_e32 v77, v29
	v_mov_b32_e32 v78, v30
	v_mov_b32_e32 v79, v31
	v_mov_b32_e32 v80, v32
	v_mov_b32_e32 v81, v33
	v_mov_b32_e32 v82, v34
	v_mov_b32_e32 v83, v35
	v_mov_b32_e32 v84, v36
	v_mov_b32_e32 v85, v37
	v_mov_b32_e32 v86, v38
	v_mov_b32_e32 v87, v39
	v_mov_b32_e32 v88, v16
	v_mov_b32_e32 v89, v17
	v_mov_b32_e32 v90, v18
	v_mov_b32_e32 v91, v19
	v_mov_b32_e32 v92, v20
	v_mov_b32_e32 v93, v21
	v_mov_b32_e32 v94, v22
	v_mov_b32_e32 v95, v23
	v_mov_b32_e32 v96, v24
	v_mov_b32_e32 v97, v25
	v_mov_b32_e32 v98, v26
	v_mov_b32_e32 v99, v27
	v_mov_b32_e32 v100, v28
	v_mov_b32_e32 v101, v29
	v_mov_b32_e32 v102, v30
	v_mov_b32_e32 v103, v31
	v_mov_b32_e32 v104, v32
	v_mov_b32_e32 v105, v33
	v_mov_b32_e32 v106, v34
	v_mov_b32_e32 v107, v35
	v_mov_b32_e32 v108, v36
	v_mov_b32_e32 v109, v37
	v_mov_b32_e32 v110, v38
	v_mov_b32_e32 v111, v39
	v_mov_b32_e32 v112, v16
	v_mov_b32_e32 v113, v17
	v_mov_b32_e32 v114, v18
	v_mov_b32_e32 v115, v19
	v_mov_b32_e32 v116, v20
	v_mov_b32_e32 v117, v21
	v_mov_b32_e32 v118, v22
	v_mov_b32_e32 v119, v23
	v_mov_b32_e32 v120, v24
	v_mov_b32_e32 v121, v25
	v_mov_b32_e32 v122, v26
	v_mov_b32_e32 v123, v27
	v_mov_b32_e32 v124, v28
	v_mov_b32_e32 v125, v29
	v_mov_b32_e32 v126, v30
	v_mov_b32_e32 v127, v31
	v_mov_b32_e32 v128, v32
	v_mov_b32_e32 v129, v33
	v_mov_b32_e32 v130, v34
	v_mov_b32_e32 v131, v35
	v_mov_b32_e32 v132, v36
	v_mov_b32_e32 v133, v37
	v_mov_b32_e32 v134, v38
	v_mov_b32_e32 v135, v39
	v_mov_b32_e32 v136, v16
	v_mov_b32_e32 v137, v17
	v_mov_b32_e32 v138, v18
	v_mov_b32_e32 v139, v19
	v_mov_b32_e32 v140, v20
	v_mov_b32_e32 v141, v21
	v_mov_b32_e32 v142, v22
	v_mov_b32_e32 v143, v23
	v_mov_b32_e32 v144, v24
	v_mov_b32_e32 v145, v25
	v_mov_b32_e32 v146, v26
	v_mov_b32_e32 v147, v27
	v_mov_b32_e32 v148, v28
	v_mov_b32_e32 v149, v29
	v_mov_b32_e32 v150, v30
	v_mov_b32_e32 v151, v31
	v_mov_b32_e32 v152, v32
	v_mov_b32_e32 v153, v33
	v_mov_b32_e32 v154, v34
	v_mov_b32_e32 v155, v35
	v_mov_b32_e32 v156, v36
	v_mov_b32_e32 v157, v37
	v_mov_b32_e32 v158, v38
	v_mov_b32_e32 v159, v39
	v_mov_b32_e32 v160, v16
	v_mov_b32_e32 v161, v17
	v_mov_b32_e32 v162, v18
	v_mov_b32_e32 v163, v19
	v_mov_b32_e32 v164, v20
	v_mov_b32_e32 v165, v21
	v_mov_b32_e32 v166, v22
	v_mov_b32_e32 v167, v23
	v_mov_b32_e32 v168, v24
	v_mov_b32_e32 v169, v25
	v_mov_b32_e32 v170, v26
	v_mov_b32_e32 v171, v27
	v_mov_b32_e32 v172, v28
	v_mov_b32_e32 v173, v29
	v_mov_b32_e32 v174, v30
	v_mov_b32_e32 v175, v31
	v_mov_b32_e32 v176, v32
	v_mov_b32_e32 v177, v33
	v_mov_b32_e32 v178, v34
	v_mov_b32_e32 v179, v35
	v_mov_b32_e32 v180, v36
	v_mov_b32_e32 v181, v37
	v_mov_b32_e32 v182, v38
	v_mov_b32_e32 v183, v39
	v_mov_b32_e32 v184, v16
	v_mov_b32_e32 v185, v17
	v_mov_b32_e32 v186, v18
	v_mov_b32_e32 v187, v19
	v_mov_b32_e32 v188, v20
	v_mov_b32_e32 v189, v21
	v_mov_b32_e32 v190, v22
	v_mov_b32_e32 v191, v23
	v_mov_b32_e32 v192, v24
	v_mov_b32_e32 v193, v25
	v_mov_b32_e32 v194, v26
	v_mov_b32_e32 v195, v27
	v_mov_b32_e32 v196, v28
	v_mov_b32_e32 v197, v29
	v_mov_b32_e32 v198, v30
	v_mov_b32_e32 v199, v31
	v_mov_b32_e32 v200, v32
	v_mov_b32_e32 v201, v33
	v_mov_b32_e32 v202, v34
	v_mov_b32_e32 v203, v35
	v_mov_b32_e32 v204, v36
	v_mov_b32_e32 v205, v37
	v_mov_b32_e32 v206, v38
	v_mov_b32_e32 v207, v39
	v_mov_b32_e32 v208, v16
	v_mov_b32_e32 v209, v17
	v_mov_b32_e32 v210, v18
	v_mov_b32_e32 v211, v19
	v_mov_b32_e32 v212, v20
	v_mov_b32_e32 v213, v21
	v_mov_b32_e32 v214, v22
	v_mov_b32_e32 v215, v23
	v_mov_b32_e32 v216, v24
	v_mov_b32_e32 v217, v25
	v_mov_b32_e32 v218, v26
	v_mov_b32_e32 v219, v27
	v_mov_b32_e32 v220, v28
	v_mov_b32_e32 v221, v29
	v_mov_b32_e32 v222, v30
	v_mov_b32_e32 v223, v31
	v_mov_b32_e32 v224, v32
	v_mov_b32_e32 v225, v33
	v_mov_b32_e32 v226, v34
	v_mov_b32_e32 v227, v35
	v_mov_b32_e32 v228, v36
	v_mov_b32_e32 v229, v37
	v_mov_b32_e32 v230, v38
	v_mov_b32_e32 v231, v39
	v_mov_b32_e32 v232, v16
	v_mov_b32_e32 v233, v17
	v_mov_b32_e32 v234, v18
	v_mov_b32_e32 v235, v19
	v_mov_b32_e32 v236, v20
	v_mov_b32_e32 v237, v21
	v_mov_b32_e32 v238, v22
	v_mov_b32_e32 v239, v23
	v_mov_b32_e32 v240, v24
	v_mov_b32_e32 v241, v25
	v_mov_b32_e32 v242, v26
	v_mov_b32_e32 v243, v27
	v_mov_b32_e32 v244, v28
	v_mov_b32_e32 v245, v29
	v_mov_b32_e32 v246, v30
	v_mov_b32_e32 v247, v31
	v_mov_b32_e32 v248, v32
	v_mov_b32_e32 v249, v33
	v_mov_b32_e32 v250, v34
	v_mov_b32_e32 v251, v35
	v_mov_b32_e32 v252, v36
	v_mov_b32_e32 v253, v37
	v_mov_b32_e32 v254, v38
	v_mov_b32_e32 v255, v39
	s_waitcnt vmcnt(5)
	s_barrier
	s_barrier
.Lfc_h1_loop:
	ds_read_b128 v[16:19], v3 offset:0
	ds_read_b128 v[20:23], v3 offset:1024
	ds_read_b128 v[24:27], v3 offset:2048
	ds_read_b128 v[28:31], v3 offset:3072
	ds_read_b128 v[32:35], v3 offset:4096
	ds_read_b128 v[36:39], v3 offset:5120
	ds_read_b128 v[40:43], v1 offset:0
	ds_read_b128 v[44:47], v1 offset:1024
	ds_read_b128 v[48:51], v1 offset:2048
	ds_read_b128 v[52:55], v1 offset:3072
	s_cmp_eq_u32 s21, 0
	s_cbranch_scc0 .Lfc_h1_nox
	s_add_u32 m0, s22, 0x14000
	s_nop 0
	global_load_lds_dwordx4 v5, s[24:25]
	s_add_u32 m0, s22, 0x14400
	s_nop 0
	global_load_lds_dwordx4 v6, s[24:25]
	s_add_u32 m0, s23, 0x14000
	s_nop 0
	global_load_lds_dwordx4 v11, s[28:29]
	s_add_u32 m0, s23, 0x14400
	s_nop 0
	global_load_lds_dwordx4 v11, s[32:33]
	s_add_u32 m0, s23, 0x14800
	s_nop 0
	global_load_lds_dwordx4 v11, s[36:37]
	s_add_u32 s24, s24, 0x80
	s_addc_u32 s25, s25, 0
	s_add_u32 s28, s28, 0x30000
	s_addc_u32 s29, s29, 0
	s_add_u32 s32, s32, 0x30000
	s_addc_u32 s33, s33, 0
	s_add_u32 s36, s36, 0x30000
	s_addc_u32 s37, s37, 0
.Lfc_h1_nox:
	s_add_u32 m0, s22, 0x1e000
	s_nop 0
	global_load_lds_dwordx4 v5, s[26:27]
	s_add_u32 m0, s22, 0x1e400
	s_nop 0
	global_load_lds_dwordx4 v6, s[26:27]
	s_add_u32 m0, s23, 0x1e000
	s_nop 0
	global_load_lds_dwordx4 v11, s[30:31]
	s_add_u32 m0, s23, 0x1e400
	s_nop 0
	global_load_lds_dwordx4 v11, s[34:35]
	s_add_u32 m0, s23, 0x1e800
	s_nop 0
	global_load_lds_dwordx4 v11, s[38:39]
	s_add_u32 s26, s26, 0x80
	s_addc_u32 s27, s27, 0
	s_add_u32 s30, s30, 0x30000
	s_addc_u32 s31, s31, 0
	s_add_u32 s34, s34, 0x30000
	s_addc_u32 s35, s35, 0
	s_add_u32 s38, s38, 0x30000
	s_addc_u32 s39, s39, 0
	s_cmp_eq_u32 s21, 3
	s_cbranch_scc1 .Lfc_sw_8
	s_cmp_eq_u32 s21, 7
	s_cbranch_scc0 .Lfc_swd_8
	s_add_u32 s28, s28, 0x180000
	s_addc_u32 s29, s29, 0
	s_add_u32 s30, s30, 0x180000
	s_addc_u32 s31, s31, 0
	s_add_u32 s32, s32, 0x180000
	s_addc_u32 s33, s33, 0
	s_add_u32 s34, s34, 0x180000
	s_addc_u32 s35, s35, 0
	s_add_u32 s36, s36, 0x180000
	s_addc_u32 s37, s37, 0
	s_add_u32 s38, s38, 0x180000
	s_addc_u32 s39, s39, 0
	s_branch .Lfc_sw2_8
